# strategy 7.4: one static s_setprio 1 for waves 4-7 at mixer-phase entry (attention/SGU units), nothing else changed
# baseline (speedup 1.0000x reference)
; #define GRID_BAR() do { XcdBarrier bb_ = bar; GAS unsigned* gb_ = (GAS unsigned*)bar.bar; asm volatile("" : "+s"(gb_), "+s"(bb_.x)); bb_.bar = (unsigned*)gb_; xcd_barrier(bb_); } while (0)
; __global__ void __launch_bounds__(NWAVES * 64, 2) mega_fwd(Args args) {
;     ...
;         if (IN(pb + 2)) for (int rep = 0; rep < REPS(3, l); ++rep) {
;             if (rep) GRID_BAR();
;             { PHASE_CTX();
;             const bf16_t* PROJ = (const bf16_t*)(ws + WS_PROJ); bf16_t* Y = (bf16_t*)(ws + WS_Y);
;             const bf16_t* mkv = (const bf16_t*)(ws + WS_MKV) + (size_t)l * MEMR * 2048;
;             gu32* qhead = (gu32*)(ws + WS_CTL) + CW_Q + 64 * (l + 2 * rep);
;             const float lam_init = l == 0 ? 0.2f : 0.35550907f;
;             for (;;) {
;                 if (tid == 0) MISC[16] = __hip_atomic_fetch_add(qhead, 1u, RLX_AGENT);
;                 __syncthreads(); const int uq = (int)MISC[16]; __syncthreads();
;                 int lane_u = lane; asm volatile("" : "+v"(lane_u));
;                 constexpr int NCONV = CONV_NCH;
;                 int u = uq; bool xtra = false; (void)xtra;
.LBB0_423:
	v_readlane_b32 s10, v253, 41
	v_readlane_b32 s0, v253, 34
	v_mov_b32_e32 v1, 0x3eb60549
	v_mov_b32_e32 v2, 0x3e4ccccd
	v_readlane_b32 s1, v253, 35
	s_mov_b32 s12, s10
	v_readlane_b32 s11, v253, 42
	v_cndmask_b32_e64 v203, v1, v2, s[0:1]
	v_writelane_b32 v253, s12, 41
	v_mov_b32_e32 v1, v0
	s_mov_b32 s11, s3
	v_writelane_b32 v253, s13, 42
	s_lshl_b64 s[6:7], s[10:11], 22
	v_readfirstlane_b32 s12, v1
	s_lshl_b32 s2, s10, 7
	s_lshl_b32 s0, s10, 8
	s_lshl_b64 s[8:9], s[10:11], 21
	s_lshl_b32 s4, s10, 10
	s_lshl_b64 s[10:11], s[10:11], 19
	v_readlane_b32 s20, v252, 6
	s_ashr_i32 s14, s12, 6
	s_cmp_gt_i32 s14, 3
	s_cbranch_scc0 .Lmix_prio_done
	s_setprio 1
.Lmix_prio_done:
	v_writelane_b32 v253, s10, 54
	v_readlane_b32 s26, v252, 12
	v_readlane_b32 s27, v252, 13
	s_lshl_b32 s13, s14, 14
	v_writelane_b32 v253, s11, 55
	s_mov_b64 s[10:11], s[26:27]
	s_add_i32 s13, s13, 0
	s_add_u32 s18, s10, 0x3c120000
	v_writelane_b32 v253, s13, 56
	s_addc_u32 s19, s11, 0
	v_writelane_b32 v253, s18, 48
	s_mov_b32 s1, s3
	s_mov_b32 s5, s3
	v_writelane_b32 v253, s19, 49
	s_add_u32 s18, s10, 0x59160000
	s_addc_u32 s19, s11, 0
	s_add_u32 s6, s10, s6
	v_writelane_b32 v253, s18, 57
	s_addc_u32 s7, s11, s7
	s_add_u32 s6, s6, 0x3b920000
	v_writelane_b32 v253, s19, 58
	v_writelane_b32 v253, s6, 59
	s_addc_u32 s6, s7, 0
	v_writelane_b32 v253, s6, 60
	s_lshl_b64 s[6:7], s[16:17], 2
	s_add_u32 s6, s10, s6
	s_addc_u32 s7, s11, s7
	s_add_u32 s6, s6, 0x2000
	s_addc_u32 s7, s7, 0
	v_writelane_b32 v253, s6, 61
	v_sub_f32_e32 v205, 1.0, v203
	v_and_b32_e32 v207, 63, v1
	v_writelane_b32 v253, s7, 62
	v_cmp_eq_u32_e64 s[6:7], 0, v1
	v_readlane_b32 s21, v252, 7
	v_readlane_b32 s22, v252, 8
	v_writelane_b32 v253, s6, 63
	v_readlane_b32 s23, v252, 9
	v_readlane_b32 s24, v252, 10
	v_writelane_b32 v254, s7, 0
	s_add_u32 s6, s10, 0x3000
	s_addc_u32 s7, s11, 0
	v_writelane_b32 v254, s6, 1
	v_readlane_b32 s25, v252, 11
	s_nop 0
	v_writelane_b32 v254, s7, 2
	s_lshl_b32 s6, s14, 2
	s_add_i32 s7, s6, 0xffffe000
	s_add_u32 s16, s10, 0x25100000
	v_writelane_b32 v254, s7, 3
	s_addc_u32 s17, s11, 0
	v_writelane_b32 v254, s16, 4
	s_nop 1
	v_writelane_b32 v254, s17, 5
	s_add_u32 s16, s10, 0x21100000
	s_addc_u32 s17, s11, 0
	v_writelane_b32 v254, s16, 6
	s_nop 1
	v_writelane_b32 v254, s17, 7
	s_add_u32 s16, s10, 0x1e100000
	s_addc_u32 s17, s11, 0
	v_writelane_b32 v254, s16, 8
	s_nop 1
	v_writelane_b32 v254, s17, 9
	s_add_u32 s16, s10, 0xe900000
	s_addc_u32 s17, s11, 0
	v_writelane_b32 v254, s16, 10
	s_nop 1
	v_writelane_b32 v254, s17, 11
	v_writelane_b32 v254, s6, 12
	s_addk_i32 s6, 0x7c00
	v_writelane_b32 v254, s6, 13
	s_add_u32 s6, s10, 0x23100000
	s_addc_u32 s7, s11, 0
	v_writelane_b32 v254, s6, 14
	s_nop 1
	v_writelane_b32 v254, s7, 15
	s_add_u32 s6, s10, 0x1f100000
	s_addc_u32 s7, s11, 0
	v_writelane_b32 v254, s6, 16
	s_nop 1
	v_writelane_b32 v254, s7, 17
	s_add_u32 s6, s10, 0x1d100000
	s_addc_u32 s7, s11, 0
	v_writelane_b32 v254, s6, 18
	s_nop 1
	v_writelane_b32 v254, s7, 19
	s_add_u32 s6, s10, 0x100000
	s_addc_u32 s7, s11, 0
	v_writelane_b32 v254, s6, 20
	s_nop 1
	v_writelane_b32 v254, s7, 21
	s_add_u32 s6, s10, 0x59120000
	v_writelane_b32 v254, s6, 22
	s_addc_u32 s6, s11, 0
	v_writelane_b32 v254, s6, 23
	v_writelane_b32 v254, s14, 24
	s_lshl_b32 s6, s14, 5
	v_writelane_b32 v254, s6, 25
	v_readlane_b32 s6, v252, 57
	v_readlane_b32 s7, v252, 58
	s_add_u32 s6, s10, s6
	s_addc_u32 s7, s11, s7
	s_add_u32 s14, s6, 0x5d160000
	s_addc_u32 s15, s7, 0
	v_writelane_b32 v254, s14, 26
	s_add_u32 s6, s6, 0x5d180000
	s_addc_u32 s7, s7, 0
	v_writelane_b32 v254, s15, 27
	v_writelane_b32 v254, s6, 28
	s_nop 1
	v_writelane_b32 v254, s7, 29
	s_add_u32 s6, s10, 0x6f660000
	v_writelane_b32 v254, s6, 30
	s_addc_u32 s6, s11, 0
	v_writelane_b32 v254, s6, 31
	s_and_b32 s6, s12, 0xffffffc0
	v_writelane_b32 v254, s6, 32
	s_add_u32 s6, s10, s8
	s_addc_u32 s7, s11, s9
	s_add_u32 s6, s6, 0x6f160000
	v_writelane_b32 v254, s6, 33
	s_addc_u32 s6, s7, 0
	v_writelane_b32 v254, s6, 34
	s_add_u32 s6, s10, 0x59161800
	s_addc_u32 s7, s11, 0
	v_writelane_b32 v254, s6, 35
	s_nop 1
	v_writelane_b32 v254, s7, 36
	s_add_u32 s6, s10, 0x6f560000
	s_addc_u32 s7, s11, 0
	v_writelane_b32 v254, s6, 37
	s_add_u32 s10, s10, 0x59161000
	s_addc_u32 s11, s11, 0
	v_writelane_b32 v254, s7, 38
	s_lshl_b64 s[6:7], s[2:3], 2
	v_writelane_b32 v254, s6, 39
	s_lshl_b64 s[0:1], s[0:1], 2
	s_nop 0
	v_writelane_b32 v254, s7, 40
	v_writelane_b32 v254, s0, 41
	s_nop 1
	v_writelane_b32 v254, s1, 42
	s_lshl_b64 s[0:1], s[4:5], 2
	v_writelane_b32 v254, s0, 43
	s_nop 1
	v_writelane_b32 v254, s1, 44
	v_writelane_b32 v254, s10, 45
	s_nop 1
	v_writelane_b32 v254, s11, 46
	s_branch .LBB0_427
